# strategy 7 (sec 7.5): the 8 v_pk_fma_f32 of the attention softmax scaling split into scalar v_fmamk_f32 (bit-identical)
# speedup vs baseline: 1.0025x; 1.0011x over previous
.LBB0_1354:
	v_cndmask_b32_e64 v211, v169, v173, s[18:19]
	v_mul_f32_e32 v148, 0xbdd53b94, v211
	v_mov_b32_e32 v149, v148
	v_fmamk_f32 v82, v82, 0x3dd53b94, v148
	v_fmamk_f32 v83, v83, 0x3dd53b94, v148
	v_fmamk_f32 v84, v84, 0x3dd53b94, v148
	v_fmamk_f32 v85, v85, 0x3dd53b94, v148
	v_fmamk_f32 v86, v86, 0x3dd53b94, v148
	v_fmamk_f32 v87, v87, 0x3dd53b94, v148
	v_fmamk_f32 v88, v88, 0x3dd53b94, v148
	v_fmamk_f32 v89, v89, 0x3dd53b94, v148
	v_fmamk_f32 v90, v90, 0x3dd53b94, v148
	v_fmamk_f32 v91, v91, 0x3dd53b94, v148
	v_fmamk_f32 v92, v92, 0x3dd53b94, v148
	v_fmamk_f32 v93, v93, 0x3dd53b94, v148
	v_fmamk_f32 v94, v94, 0x3dd53b94, v148
	v_fmamk_f32 v95, v95, 0x3dd53b94, v148
	v_fmamk_f32 v96, v96, 0x3dd53b94, v148
	v_fmac_f32_e32 v149, 0x3dd53b94, v97
	v_exp_f32_e32 v169, v82
	v_exp_f32_e32 v191, v83
	v_exp_f32_e32 v170, v84
	v_exp_f32_e32 v192, v85
	v_exp_f32_e32 v190, v86
	v_exp_f32_e32 v193, v87
	v_exp_f32_e32 v171, v88
	v_exp_f32_e32 v189, v89
	v_exp_f32_e32 v173, v90
	v_exp_f32_e32 v175, v91
	v_exp_f32_e32 v174, v92
	v_exp_f32_e32 v188, v93
	v_exp_f32_e32 v164, v94
	v_exp_f32_e32 v166, v95
	v_exp_f32_e32 v165, v96
	v_exp_f32_e32 v167, v149
	v_fmamk_f32 v163, v67, 0x3dd53b94, v148
	v_fmamk_f32 v162, v66, 0x3dd53b94, v148
	v_add_f32_e32 v66, v212, v213
	v_fmac_f32_e32 v66, v210, v199
	v_add_f32_e32 v199, v229, v230
	s_add_i32 s8, s8, 2
	v_fmamk_f32 v161, v69, 0x3dd53b94, v148
	v_fmamk_f32 v160, v68, 0x3dd53b94, v148
	v_fmamk_f32 v157, v71, 0x3dd53b94, v148
	v_fmamk_f32 v156, v70, 0x3dd53b94, v148
	v_fmamk_f32 v153, v73, 0x3dd53b94, v148
	v_fmamk_f32 v152, v72, 0x3dd53b94, v148
	v_fmamk_f32 v151, v75, 0x3dd53b94, v148
	v_fmamk_f32 v150, v74, 0x3dd53b94, v148
	v_fmamk_f32 v159, v77, 0x3dd53b94, v148
	v_fmamk_f32 v158, v76, 0x3dd53b94, v148
	v_fmamk_f32 v155, v79, 0x3dd53b94, v148
	v_fmamk_f32 v154, v78, 0x3dd53b94, v148
	v_fmamk_f32 v149, v81, 0x3dd53b94, v148
	v_fmamk_f32 v148, v80, 0x3dd53b94, v148
	v_fmac_f32_e32 v199, v66, v172
	s_cmp_ge_u32 s8, s3
	s_waitcnt vmcnt(0) lgkmcnt(0)
	s_barrier
	s_cbranch_scc1 .LBB0_1356
	v_mov_b32_e32 v227, 0x3200
	v_mov_b32_e32 v210, v168
	s_branch .LBB0_1344
